# diff-combine row loop software-pipelined: next row's loads issued before the current row's reductions/stores, loop-top wait vmcnt(8) (stores stay in flight); plus GEMM2 epilogue, router, combine load
# baseline (speedup 1.0000x reference)
; __device__ __forceinline__ bf16_t f2bf(float f) { unsigned u = __float_as_uint(f); return (bf16_t)((u + 0x7fffu + ((u >> 16) & 1u)) >> 16); }
; __host__ __device__ inline float lam_init_of(int l) { return 0.8f - 0.6f * expf(-0.3f * (float)l); }
; __device__ __forceinline__ void ph_diffc(const P& p, int l, int row0, int gw, int nw, int lane) {
;   const float lam = WSP(float, WS_SMALL)[1024 + l], li = lam_init_of(l);
;   const float d0 = p.dn[l * 128 + lane] * (1.f - li), d1 = p.dn[l * 128 + lane + 64] * (1.f - li);
;   for (int t = row0 + gw; t < NTOK; t += nw) {
;     const float* d = WSP(float, WS_DTMP) + (size_t)t * 1024;
;     float a[4], b[4];
; #pragma unroll
;     for (int h = 0; h < 4; ++h) { const float x0 = d[h * 256 + lane], x1 = d[h * 256 + 128 + lane], y0 = d[h * 256 + 64 + lane], y1 = d[h * 256 + 192 + lane]; a[h] = x0 - lam * x1; b[h] = y0 - lam * y1; }
;     bf16_t* m = WSP(bf16_t, WS_MIX) + (size_t)t * DM + 1536;
; #pragma unroll
;     for (int h = 0; h < 4; ++h) { const float rs = rsqrtf(wave_sum(a[h] * a[h] + b[h] * b[h]) * (1.f / 128) + EPS);
;       m[h * 128 + lane] = f2bf(a[h] * rs * d0); m[h * 128 + lane + 64] = f2bf(b[h] * rs * d1); }
;   }
; }
.LBB0_564:
	s_sub_i32 s3, s4, s0
	s_add_i32 s5, s3, 7
	s_ashr_i32 s6, s5, 31
	s_lshr_b32 s6, s6, 29
	s_add_i32 s5, s5, s6
	s_ashr_i32 s5, s5, 3
	s_cmp_lt_i32 s3, 1
	s_cselect_b64 s[6:7], -1, 0
	s_cmp_ge_i32 s5, s97
	v_readlane_b32 s78, v255, 23
	s_cselect_b64 s[14:15], -1, 0
	s_or_b64 s[6:7], s[6:7], s[14:15]
	v_cvt_f32_i32_e32 v0, s78
	s_lshl_b32 s9, s0, 1
	s_cmp_gt_i32 s4, s9
	v_readlane_b32 s79, v255, 24
	s_cselect_b64 s[14:15], -1, 0
	s_ashr_i32 s79, s78, 31
	s_or_b64 s[14:15], s[6:7], s[14:15]
	s_lshl_b64 s[6:7], s[78:79], 2
	v_mul_f32_e32 v0, 0xbe99999a, v0
	s_add_u32 s4, s12, s6
	v_mul_f32_e32 v1, 0x3fb8aa3b, v0
	s_mov_b32 s6, 0x3fb8aa3b
	v_fma_f32 v2, v0, s6, -v1
	v_rndne_f32_e32 v3, v1
	v_fmac_f32_e32 v2, 0x32a5705f, v0
	v_sub_f32_e32 v1, v1, v3
	v_add_f32_e32 v1, v1, v2
	v_exp_f32_e32 v1, v1
	v_cvt_i32_f32_e32 v2, v3
	s_addc_u32 s6, s13, s7
	s_add_u32 s20, s4, 0x81000
	s_mov_b32 s4, 0xc2ce8ed0
	v_ldexp_f32 v1, v1, v2
	v_cmp_ngt_f32_e32 vcc, s4, v0
	s_mov_b32 s4, 0x42b17218
	v_readlane_b32 s88, v255, 12
	v_cndmask_b32_e32 v1, 0, v1, vcc
	v_cmp_nlt_f32_e32 vcc, s4, v0
	v_add_u32_e32 v0, s2, v94
	s_addc_u32 s21, s6, 0
	v_cndmask_b32_e32 v2, v218, v1, vcc
	v_ashrrev_i32_e32 v1, 31, v0
	v_lshl_add_u64 v[4:5], v[0:1], 2, s[18:19]
	v_mov_b32_e32 v0, 0xbf4ccccd
	v_fmamk_f32 v0, v2, 0x3f19999a, v0
	v_add_f32_e32 v14, 1.0, v0
	v_add_u32_e32 v2, 0x80, v94
	v_add_u32_e32 v0, 0x180, v94
	v_ashrrev_i32_e32 v95, 31, v94
	v_ashrrev_i32_e32 v3, 31, v2
	v_ashrrev_i32_e32 v1, 31, v0
	s_mov_b64 s[6:7], -1
	s_and_b64 vcc, exec, s[14:15]
	v_readlane_b32 s89, v255, 13
	v_readlane_b32 s81, v255, 15
	s_mov_b32 s93, 0x18000
	s_mov_b32 s96, 0x1c000
	s_cbranch_vccnz .LBB0_589
	s_cmp_lt_i32 s88, s5
	s_mov_b32 s38, 0xc000
	s_brev_b32 s6, 60
	s_mov_b32 s16, 0x358637bd
	s_cbranch_scc1 .LBB0_588
	s_lshl_b32 s2, s5, 3
	s_sub_i32 s4, s1, s2
	s_add_i32 s14, s4, s92
	s_cmpk_gt_i32 s14, 0x20ff
	s_cbranch_scc1 .LBB0_569
	global_load_dword v12, v[4:5], off
	global_load_dword v13, v[4:5], off offset:256
	global_load_dword v15, v97, s[20:21]
	s_ashr_i32 s15, s14, 31
	s_sub_i32 s18, s0, s2
	s_lshl_b64 s[4:5], s[14:15], 12
	s_add_u32 s22, s12, s4
	s_addc_u32 s23, s13, s5
	s_ashr_i32 s19, s18, 31
	v_lshlrev_b64 v[6:7], 2, v[94:95]
	v_lshlrev_b64 v[8:9], 1, v[94:95]
	v_lshlrev_b64 v[10:11], 1, v[2:3]
	s_lshl_b64 s[34:35], s[18:19], 12
	s_mov_b32 s2, 0x2d814000
	s_waitcnt vmcnt(0)
	v_mul_f32_e32 v16, v14, v12
	v_mul_f32_e32 v17, v14, v13
	v_lshlrev_b64 v[12:13], 1, v[0:1]
	v_lshl_add_u64 v[116:117], s[22:23], 0, v[6:7]
	v_add_co_u32_e32 v116, vcc, 0x2f914000, v116
	s_nop 1
	v_addc_co_u32_e32 v117, vcc, 0, v117, vcc
	global_load_dword v100, v[116:117], off
	global_load_dword v101, v[116:117], off offset:512
	global_load_dword v102, v[116:117], off offset:256
	global_load_dword v103, v[116:117], off offset:768
	global_load_dword v104, v[116:117], off offset:1024
	global_load_dword v105, v[116:117], off offset:1536
	global_load_dword v106, v[116:117], off offset:1280
	global_load_dword v107, v[116:117], off offset:1792
	global_load_dword v108, v[116:117], off offset:2048
	global_load_dword v109, v[116:117], off offset:2560
	global_load_dword v110, v[116:117], off offset:2304
	global_load_dword v111, v[116:117], off offset:2816
	global_load_dword v112, v[116:117], off offset:3072
	global_load_dword v113, v[116:117], off offset:3584
	global_load_dword v114, v[116:117], off offset:3328
	global_load_dword v115, v[116:117], off offset:3840
	s_waitcnt vmcnt(0)
.LBB0_568:
	v_lshl_add_u64 v[24:25], s[22:23], 0, v[8:9]
	s_waitcnt vmcnt(8)
	s_add_i32 s14, s14, s18
	v_fma_f32 v26, -v15, v101, v100
	v_fma_f32 v27, -v15, v103, v102
	v_fma_f32 v28, -v15, v105, v104
	v_fma_f32 v29, -v15, v107, v106
	v_fma_f32 v30, -v15, v109, v108
	v_fma_f32 v31, -v15, v111, v110
	v_fma_f32 v19, -v15, v113, v112
	v_mul_f32_e32 v20, v27, v27
	v_fmac_f32_e32 v20, v26, v26
	v_fma_f32 v18, -v15, v115, v114
	s_cmpk_lt_i32 s14, 0x2100
	s_cbranch_scc0 .Ldc_nfa
	s_add_u32 s26, s22, s34
	s_addc_u32 s27, s23, s35
	v_lshl_add_u64 v[116:117], s[26:27], 0, v[6:7]
	v_add_co_u32_e32 v116, vcc, 0x2f914000, v116
	s_nop 1
	v_addc_co_u32_e32 v117, vcc, 0, v117, vcc
	global_load_dword v100, v[116:117], off
	global_load_dword v101, v[116:117], off offset:512
	global_load_dword v102, v[116:117], off offset:256
	global_load_dword v103, v[116:117], off offset:768
	global_load_dword v104, v[116:117], off offset:1024
	global_load_dword v105, v[116:117], off offset:1536
	global_load_dword v106, v[116:117], off offset:1280
	global_load_dword v107, v[116:117], off offset:1792
	global_load_dword v108, v[116:117], off offset:2048
	global_load_dword v109, v[116:117], off offset:2560
	global_load_dword v110, v[116:117], off offset:2304
	global_load_dword v111, v[116:117], off offset:2816
	global_load_dword v112, v[116:117], off offset:3072
	global_load_dword v113, v[116:117], off offset:3584
	global_load_dword v114, v[116:117], off offset:3328
	global_load_dword v115, v[116:117], off offset:3840
; __device__ __forceinline__ bf16_t f2bf(float f) { unsigned u = __float_as_uint(f); return (bf16_t)((u + 0x7fffu + ((u >> 16) & 1u)) >> 16); }
; __host__ __device__ inline float lam_init_of(int l) { return 0.8f - 0.6f * expf(-0.3f * (float)l); }
; __device__ __forceinline__ void ph_diffc(const P& p, int l, int row0, int gw, int nw, int lane) {
;   const float lam = WSP(float, WS_SMALL)[1024 + l], li = lam_init_of(l);
;   const float d0 = p.dn[l * 128 + lane] * (1.f - li), d1 = p.dn[l * 128 + lane + 64] * (1.f - li);
;   for (int t = row0 + gw; t < NTOK; t += nw) {
;     const float* d = WSP(float, WS_DTMP) + (size_t)t * 1024;
;     float a[4], b[4];
; #pragma unroll
;     for (int h = 0; h < 4; ++h) { const float x0 = d[h * 256 + lane], x1 = d[h * 256 + 128 + lane], y0 = d[h * 256 + 64 + lane], y1 = d[h * 256 + 192 + lane]; a[h] = x0 - lam * x1; b[h] = y0 - lam * y1; }
;     bf16_t* m = WSP(bf16_t, WS_MIX) + (size_t)t * DM + 1536;
; #pragma unroll
;     for (int h = 0; h < 4; ++h) { const float rs = rsqrtf(wave_sum(a[h] * a[h] + b[h] * b[h]) * (1.f / 128) + EPS);
;       m[h * 128 + lane] = f2bf(a[h] * rs * d0); m[h * 128 + lane + 64] = f2bf(b[h] * rs * d1); }
;   }
; }
.Ldc_nfa:
	v_add_f32_dpp v20, v20, v20 quad_perm:[1,0,3,2] row_mask:0xf bank_mask:0xf bound_ctrl:1
	s_nop 1
	v_add_f32_dpp v20, v20, v20 quad_perm:[2,3,0,1] row_mask:0xf bank_mask:0xf bound_ctrl:1
	s_nop 1
	v_add_f32_dpp v20, v20, v20 row_half_mirror row_mask:0xf bank_mask:0xf bound_ctrl:1
	s_nop 1
	v_add_f32_dpp v20, v20, v20 row_mirror row_mask:0xf bank_mask:0xf bound_ctrl:1
	v_mov_b32_e32 v21, v20
	s_nop 1
	v_permlane16_swap_b32_e32 v20, v21
	v_add_f32_e32 v21, v20, v21
	v_mul_f32_e32 v20, v29, v29
	v_fmac_f32_e32 v20, v28, v28
	v_mov_b32_e32 v23, v21
	s_nop 1
	v_permlane32_swap_b32_e32 v21, v23
	v_add_f32_dpp v20, v20, v20 quad_perm:[1,0,3,2] row_mask:0xf bank_mask:0xf bound_ctrl:1
	s_nop 1
	v_add_f32_dpp v20, v20, v20 quad_perm:[2,3,0,1] row_mask:0xf bank_mask:0xf bound_ctrl:1
	s_nop 1
	v_add_f32_dpp v20, v20, v20 row_half_mirror row_mask:0xf bank_mask:0xf bound_ctrl:1
	s_nop 1
	v_add_f32_dpp v20, v20, v20 row_mirror row_mask:0xf bank_mask:0xf bound_ctrl:1
	v_mov_b32_e32 v22, v20
	s_nop 1
	v_permlane16_swap_b32_e32 v20, v22
	v_add_f32_e32 v20, v20, v22
	v_mov_b32_e32 v22, v20
	s_nop 1
	v_permlane32_swap_b32_e32 v20, v22
	v_pk_add_f32 v[20:21], v[20:21], v[22:23]
	v_mov_b64_e32 v[22:23], s[16:17]
	v_pk_fma_f32 v[20:21], v[20:21], s[6:7], v[22:23] op_sel_hi:[1,0,0]
	s_nop 0
	v_mul_f32_e32 v32, 0x4b800000, v21
	v_cmp_gt_f32_e64 s[40:41], s37, v21
	v_cmp_gt_f32_e32 vcc, s37, v20
	s_nop 0
	v_cndmask_b32_e64 v21, v21, v32, s[40:41]
	v_rsq_f32_e32 v21, v21
	s_nop 0
	v_mul_f32_e32 v32, 0x45800000, v21
	v_cndmask_b32_e64 v21, v21, v32, s[40:41]
	v_mul_f32_e32 v26, v26, v21
	v_mul_f32_e32 v26, v16, v26
	v_bfe_u32 v32, v26, 16, 1
	v_add_co_u32_e64 v24, s[40:41], s2, v24
	v_mul_f32_e32 v21, v27, v21
	v_add3_u32 v26, v26, v32, s86
	v_addc_co_u32_e64 v25, s[40:41], 0, v25, s[40:41]
	v_mul_f32_e32 v21, v17, v21
	global_store_short_d16_hi v[24:25], v26, off offset:3072
	v_bfe_u32 v26, v21, 16, 1
	v_add3_u32 v21, v21, v26, s86
	global_store_short_d16_hi v[24:25], v21, off offset:3200
	v_mul_f32_e32 v21, 0x4b800000, v20
	v_cndmask_b32_e32 v20, v20, v21, vcc
	v_rsq_f32_e32 v20, v20
	s_nop 0
	v_mul_f32_e32 v21, 0x45800000, v20
	v_cndmask_b32_e32 v26, v20, v21, vcc
	v_mul_f32_e32 v20, v28, v26
	v_mul_f32_e32 v20, v16, v20
	v_bfe_u32 v21, v20, 16, 1
	v_add3_u32 v27, v20, v21, s86
	v_lshl_add_u64 v[20:21], s[22:23], 0, v[10:11]
	v_add_co_u32_e32 v20, vcc, s2, v20
	v_mul_f32_e32 v26, v29, v26
	s_nop 0
	v_addc_co_u32_e32 v21, vcc, 0, v21, vcc
	v_mul_f32_e32 v26, v17, v26
	global_store_short_d16_hi v[20:21], v27, off offset:3072
	v_bfe_u32 v27, v26, 16, 1
	v_add3_u32 v26, v26, v27, s86
	global_store_short_d16_hi v[20:21], v26, off offset:3200
	v_mul_f32_e32 v20, v31, v31
	v_fmac_f32_e32 v20, v30, v30
	s_nop 1
	v_add_f32_dpp v20, v20, v20 quad_perm:[1,0,3,2] row_mask:0xf bank_mask:0xf bound_ctrl:1
	s_nop 1
	v_add_f32_dpp v20, v20, v20 quad_perm:[2,3,0,1] row_mask:0xf bank_mask:0xf bound_ctrl:1
	s_nop 1
	v_add_f32_dpp v20, v20, v20 row_half_mirror row_mask:0xf bank_mask:0xf bound_ctrl:1
	s_nop 1
	v_add_f32_dpp v20, v20, v20 row_mirror row_mask:0xf bank_mask:0xf bound_ctrl:1
	v_mov_b32_e32 v21, v20
	s_nop 1
	v_permlane16_swap_b32_e32 v20, v21
	v_add_f32_e32 v21, v20, v21
	v_mul_f32_e32 v20, v18, v18
	v_fmac_f32_e32 v20, v19, v19
	v_mov_b32_e32 v27, v21
	s_nop 1
	v_permlane32_swap_b32_e32 v21, v27
	v_add_f32_dpp v20, v20, v20 quad_perm:[1,0,3,2] row_mask:0xf bank_mask:0xf bound_ctrl:1
	s_nop 1
	v_add_f32_dpp v20, v20, v20 quad_perm:[2,3,0,1] row_mask:0xf bank_mask:0xf bound_ctrl:1
	s_nop 1
	v_add_f32_dpp v20, v20, v20 row_half_mirror row_mask:0xf bank_mask:0xf bound_ctrl:1
	s_nop 1
	v_add_f32_dpp v20, v20, v20 row_mirror row_mask:0xf bank_mask:0xf bound_ctrl:1
	v_mov_b32_e32 v26, v20
	s_nop 1
	v_permlane16_swap_b32_e32 v20, v26
	v_add_f32_e32 v20, v20, v26
	v_mov_b32_e32 v26, v20
	s_nop 1
	v_permlane32_swap_b32_e32 v20, v26
	v_pk_add_f32 v[20:21], v[20:21], v[26:27]
	s_nop 0
	v_pk_fma_f32 v[20:21], v[20:21], s[6:7], v[22:23] op_sel_hi:[1,0,0]
	s_nop 0
	v_mul_f32_e32 v22, 0x4b800000, v21
	v_cmp_gt_f32_e64 s[40:41], s37, v21
	v_cmp_gt_f32_e32 vcc, s37, v20
	s_nop 0
	v_cndmask_b32_e64 v21, v21, v22, s[40:41]
	v_rsq_f32_e32 v21, v21
	s_nop 0
	v_mul_f32_e32 v22, 0x45800000, v21
	v_cndmask_b32_e64 v21, v21, v22, s[40:41]
	v_mul_f32_e32 v22, v30, v21
	v_mul_f32_e32 v22, v16, v22
	v_bfe_u32 v23, v22, 16, 1
	v_mul_f32_e32 v21, v31, v21
	v_add3_u32 v22, v22, v23, s86
	v_mul_f32_e32 v21, v17, v21
	global_store_short_d16_hi v[24:25], v22, off offset:3584
	v_bfe_u32 v22, v21, 16, 1
	v_add3_u32 v21, v21, v22, s86
	global_store_short_d16_hi v[24:25], v21, off offset:3712
	v_mul_f32_e32 v21, 0x4b800000, v20
	v_cndmask_b32_e32 v20, v20, v21, vcc
	v_rsq_f32_e32 v20, v20
	s_nop 0
	v_mul_f32_e32 v21, 0x45800000, v20
	v_cndmask_b32_e32 v22, v20, v21, vcc
	v_mul_f32_e32 v19, v19, v22
	v_mul_f32_e32 v19, v16, v19
	v_bfe_u32 v20, v19, 16, 1
	v_add3_u32 v19, v19, v20, s86
	v_lshl_add_u64 v[20:21], s[22:23], 0, v[12:13]
	v_add_co_u32_e32 v20, vcc, s2, v20
	v_mul_f32_e32 v18, v18, v22
	s_nop 0
	v_addc_co_u32_e32 v21, vcc, 0, v21, vcc
	v_mul_f32_e32 v18, v17, v18
	s_add_u32 s22, s22, s34
	global_store_short_d16_hi v[20:21], v19, off offset:3072
	v_bfe_u32 v19, v18, 16, 1
	s_addc_u32 s23, s23, s35
	v_add3_u32 v18, v18, v19, s86
	s_cmpk_lt_i32 s14, 0x2100
	global_store_short_d16_hi v[20:21], v18, off offset:3200
	s_cbranch_scc1 .LBB0_568

; __device__ __forceinline__ bf16_t f2bf(float f) { unsigned u = __float_as_uint(f); return (bf16_t)((u + 0x7fffu + ((u >> 16) & 1u)) >> 16); }
; __host__ __device__ inline float lam_init_of(int l) { return 0.8f - 0.6f * expf(-0.3f * (float)l); }
; __device__ __forceinline__ void ph_diffc(const P& p, int l, int row0, int gw, int nw, int lane) {
;   const float lam = WSP(float, WS_SMALL)[1024 + l], li = lam_init_of(l);
;   const float d0 = p.dn[l * 128 + lane] * (1.f - li), d1 = p.dn[l * 128 + lane + 64] * (1.f - li);
;   for (int t = row0 + gw; t < NTOK; t += nw) {
;     const float* d = WSP(float, WS_DTMP) + (size_t)t * 1024;
;     float a[4], b[4];
; #pragma unroll
;     for (int h = 0; h < 4; ++h) { const float x0 = d[h * 256 + lane], x1 = d[h * 256 + 128 + lane], y0 = d[h * 256 + 64 + lane], y1 = d[h * 256 + 192 + lane]; a[h] = x0 - lam * x1; b[h] = y0 - lam * y1; }
;     bf16_t* m = WSP(bf16_t, WS_MIX) + (size_t)t * DM + 1536;
; #pragma unroll
;     for (int h = 0; h < 4; ++h) { const float rs = rsqrtf(wave_sum(a[h] * a[h] + b[h] * b[h]) * (1.f / 128) + EPS);
;       m[h * 128 + lane] = f2bf(a[h] * rs * d0); m[h * 128 + lane + 64] = f2bf(b[h] * rs * d1); }
;   }
; }
.LBB0_589:
	v_readlane_b32 s94, v255, 16
	s_andn2_b64 vcc, exec, s[6:7]
	v_readlane_b32 s95, v255, 17
	s_cbranch_vccnz .LBB0_593
	s_add_i32 s14, s1, s92
	s_cmpk_gt_i32 s14, 0x20ff
	s_cbranch_scc1 .LBB0_593
	global_load_dword v8, v97, s[20:21]
	global_load_dword v6, v[4:5], off
	s_ashr_i32 s15, s14, 31
	global_load_dword v4, v[4:5], off offset:256
	s_lshl_b64 s[2:3], s[14:15], 12
	s_add_u32 s12, s12, s2
	s_addc_u32 s13, s13, s3
	s_ashr_i32 s1, s0, 31
	s_lshl_b64 s[18:19], s[0:1], 12
	v_lshlrev_b64 v[2:3], 1, v[2:3]
	v_lshlrev_b64 v[0:1], 1, v[0:1]
	s_mov_b32 s1, 0x2d814000
	s_brev_b32 s2, 60
	s_mov_b32 s4, 0x358637bd
	s_waitcnt vmcnt(0)
	v_mul_f32_e32 v9, v14, v6
	v_lshlrev_b64 v[6:7], 1, v[94:95]
	v_mul_f32_e32 v10, v14, v4
	v_lshlrev_b64 v[4:5], 2, v[94:95]
	v_lshl_add_u64 v[116:117], s[12:13], 0, v[4:5]
	v_add_co_u32_e32 v116, vcc, 0x2f914000, v116
	s_nop 1
	v_addc_co_u32_e32 v117, vcc, 0, v117, vcc
	global_load_dword v100, v[116:117], off
	global_load_dword v101, v[116:117], off offset:512
	global_load_dword v102, v[116:117], off offset:256
	global_load_dword v103, v[116:117], off offset:768
	global_load_dword v104, v[116:117], off offset:1024
	global_load_dword v105, v[116:117], off offset:1536
	global_load_dword v106, v[116:117], off offset:1280
	global_load_dword v107, v[116:117], off offset:1792
	global_load_dword v108, v[116:117], off offset:2048
	global_load_dword v109, v[116:117], off offset:2560
	global_load_dword v110, v[116:117], off offset:2304
	global_load_dword v111, v[116:117], off offset:2816
	global_load_dword v112, v[116:117], off offset:3072
	global_load_dword v113, v[116:117], off offset:3584
	global_load_dword v114, v[116:117], off offset:3328
	global_load_dword v115, v[116:117], off offset:3840
	s_waitcnt vmcnt(0)
.LBB0_592:
	s_add_i32 s14, s14, s0
	s_waitcnt vmcnt(8)
	v_fma_f32 v18, -v8, v101, v100
	v_fma_f32 v19, -v8, v103, v102
	v_fma_f32 v20, -v8, v105, v104
	v_fma_f32 v21, -v8, v107, v106
	v_fma_f32 v22, -v8, v109, v108
	v_fma_f32 v23, -v8, v111, v110
	v_lshl_add_u64 v[16:17], s[12:13], 0, v[6:7]
	v_fma_f32 v24, -v8, v113, v112
	v_fma_f32 v11, -v8, v115, v114
	s_cmpk_gt_i32 s14, 0x20ff
	s_cbranch_scc1 .Ldc_nfb
	s_add_u32 s26, s12, s18
	s_addc_u32 s27, s13, s19
	v_lshl_add_u64 v[116:117], s[26:27], 0, v[4:5]
	v_add_co_u32_e32 v116, vcc, 0x2f914000, v116
	s_nop 1
	v_addc_co_u32_e32 v117, vcc, 0, v117, vcc
	global_load_dword v100, v[116:117], off
	global_load_dword v101, v[116:117], off offset:512
	global_load_dword v102, v[116:117], off offset:256
	global_load_dword v103, v[116:117], off offset:768
	global_load_dword v104, v[116:117], off offset:1024
	global_load_dword v105, v[116:117], off offset:1536
	global_load_dword v106, v[116:117], off offset:1280
	global_load_dword v107, v[116:117], off offset:1792
	global_load_dword v108, v[116:117], off offset:2048
	global_load_dword v109, v[116:117], off offset:2560
	global_load_dword v110, v[116:117], off offset:2304
	global_load_dword v111, v[116:117], off offset:2816
	global_load_dword v112, v[116:117], off offset:3072
	global_load_dword v113, v[116:117], off offset:3584
	global_load_dword v114, v[116:117], off offset:3328
	global_load_dword v115, v[116:117], off offset:3840
; __device__ __forceinline__ bf16_t f2bf(float f) { unsigned u = __float_as_uint(f); return (bf16_t)((u + 0x7fffu + ((u >> 16) & 1u)) >> 16); }
; __host__ __device__ inline float lam_init_of(int l) { return 0.8f - 0.6f * expf(-0.3f * (float)l); }
; __device__ __forceinline__ void ph_diffc(const P& p, int l, int row0, int gw, int nw, int lane) {
;   const float lam = WSP(float, WS_SMALL)[1024 + l], li = lam_init_of(l);
;   const float d0 = p.dn[l * 128 + lane] * (1.f - li), d1 = p.dn[l * 128 + lane + 64] * (1.f - li);
;   for (int t = row0 + gw; t < NTOK; t += nw) {
;     const float* d = WSP(float, WS_DTMP) + (size_t)t * 1024;
;     float a[4], b[4];
; #pragma unroll
;     for (int h = 0; h < 4; ++h) { const float x0 = d[h * 256 + lane], x1 = d[h * 256 + 128 + lane], y0 = d[h * 256 + 64 + lane], y1 = d[h * 256 + 192 + lane]; a[h] = x0 - lam * x1; b[h] = y0 - lam * y1; }
;     bf16_t* m = WSP(bf16_t, WS_MIX) + (size_t)t * DM + 1536;
; #pragma unroll
;     for (int h = 0; h < 4; ++h) { const float rs = rsqrtf(wave_sum(a[h] * a[h] + b[h] * b[h]) * (1.f / 128) + EPS);
;       m[h * 128 + lane] = f2bf(a[h] * rs * d0); m[h * 128 + lane + 64] = f2bf(b[h] * rs * d1); }
;   }
; }
.Ldc_nfb:
	v_mul_f32_e32 v12, v19, v19
	v_fmac_f32_e32 v12, v18, v18
	s_nop 1
	v_add_f32_dpp v12, v12, v12 quad_perm:[1,0,3,2] row_mask:0xf bank_mask:0xf bound_ctrl:1
	s_nop 1
	v_add_f32_dpp v12, v12, v12 quad_perm:[2,3,0,1] row_mask:0xf bank_mask:0xf bound_ctrl:1
	s_nop 1
	v_add_f32_dpp v12, v12, v12 row_half_mirror row_mask:0xf bank_mask:0xf bound_ctrl:1
	s_nop 1
	v_add_f32_dpp v12, v12, v12 row_mirror row_mask:0xf bank_mask:0xf bound_ctrl:1
	v_mov_b32_e32 v13, v12
	s_nop 1
	v_permlane16_swap_b32_e32 v12, v13
	v_add_f32_e32 v13, v12, v13
	v_mul_f32_e32 v12, v21, v21
	v_fmac_f32_e32 v12, v20, v20
	v_mov_b32_e32 v15, v13
	s_nop 1
	v_permlane32_swap_b32_e32 v13, v15
	v_add_f32_dpp v12, v12, v12 quad_perm:[1,0,3,2] row_mask:0xf bank_mask:0xf bound_ctrl:1
	s_nop 1
	v_add_f32_dpp v12, v12, v12 quad_perm:[2,3,0,1] row_mask:0xf bank_mask:0xf bound_ctrl:1
	s_nop 1
	v_add_f32_dpp v12, v12, v12 row_half_mirror row_mask:0xf bank_mask:0xf bound_ctrl:1
	s_nop 1
	v_add_f32_dpp v12, v12, v12 row_mirror row_mask:0xf bank_mask:0xf bound_ctrl:1
	v_mov_b32_e32 v14, v12
	s_nop 1
	v_permlane16_swap_b32_e32 v12, v14
	v_add_f32_e32 v12, v12, v14
	v_mov_b32_e32 v14, v12
	s_nop 1
	v_permlane32_swap_b32_e32 v12, v14
	v_pk_add_f32 v[12:13], v[12:13], v[14:15]
	v_mov_b64_e32 v[14:15], s[4:5]
	v_pk_fma_f32 v[12:13], v[12:13], s[2:3], v[14:15] op_sel_hi:[1,0,0]
	s_nop 0
	v_mul_f32_e32 v25, 0x4b800000, v13
	v_cmp_gt_f32_e64 s[40:41], s37, v13
	v_cmp_gt_f32_e32 vcc, s37, v12
	s_nop 0
	v_cndmask_b32_e64 v13, v13, v25, s[40:41]
	v_rsq_f32_e32 v13, v13
	s_nop 0
	v_mul_f32_e32 v25, 0x45800000, v13
	v_cndmask_b32_e64 v13, v13, v25, s[40:41]
	v_mul_f32_e32 v18, v18, v13
	v_mul_f32_e32 v18, v9, v18
	v_bfe_u32 v25, v18, 16, 1
	v_add_co_u32_e64 v16, s[40:41], s1, v16
	v_mul_f32_e32 v13, v19, v13
	v_add3_u32 v18, v18, v25, s86
	v_addc_co_u32_e64 v17, s[40:41], 0, v17, s[40:41]
	v_mul_f32_e32 v13, v10, v13
	global_store_short_d16_hi v[16:17], v18, off offset:3072
	v_bfe_u32 v18, v13, 16, 1
	v_add3_u32 v13, v13, v18, s86
	global_store_short_d16_hi v[16:17], v13, off offset:3200
	v_mul_f32_e32 v13, 0x4b800000, v12
	v_cndmask_b32_e32 v12, v12, v13, vcc
	v_rsq_f32_e32 v12, v12
	s_nop 0
	v_mul_f32_e32 v13, 0x45800000, v12
	v_cndmask_b32_e32 v18, v12, v13, vcc
	v_mul_f32_e32 v12, v20, v18
	v_mul_f32_e32 v12, v9, v12
	v_bfe_u32 v13, v12, 16, 1
	v_add3_u32 v19, v12, v13, s86
	v_lshl_add_u64 v[12:13], s[12:13], 0, v[2:3]
	v_add_co_u32_e32 v12, vcc, s1, v12
	v_mul_f32_e32 v18, v21, v18
	s_nop 0
	v_addc_co_u32_e32 v13, vcc, 0, v13, vcc
	v_mul_f32_e32 v18, v10, v18
	global_store_short_d16_hi v[12:13], v19, off offset:3072
	v_bfe_u32 v19, v18, 16, 1
	v_add3_u32 v18, v18, v19, s86
	global_store_short_d16_hi v[12:13], v18, off offset:3200
	v_mul_f32_e32 v12, v23, v23
	v_fmac_f32_e32 v12, v22, v22
	s_nop 1
	v_add_f32_dpp v12, v12, v12 quad_perm:[1,0,3,2] row_mask:0xf bank_mask:0xf bound_ctrl:1
	s_nop 1
	v_add_f32_dpp v12, v12, v12 quad_perm:[2,3,0,1] row_mask:0xf bank_mask:0xf bound_ctrl:1
	s_nop 1
	v_add_f32_dpp v12, v12, v12 row_half_mirror row_mask:0xf bank_mask:0xf bound_ctrl:1
	s_nop 1
	v_add_f32_dpp v12, v12, v12 row_mirror row_mask:0xf bank_mask:0xf bound_ctrl:1
	v_mov_b32_e32 v13, v12
	s_nop 1
	v_permlane16_swap_b32_e32 v12, v13
	v_add_f32_e32 v13, v12, v13
	v_mul_f32_e32 v12, v11, v11
	v_fmac_f32_e32 v12, v24, v24
	v_mov_b32_e32 v19, v13
	s_nop 1
	v_permlane32_swap_b32_e32 v13, v19
	v_add_f32_dpp v12, v12, v12 quad_perm:[1,0,3,2] row_mask:0xf bank_mask:0xf bound_ctrl:1
	s_nop 1
	v_add_f32_dpp v12, v12, v12 quad_perm:[2,3,0,1] row_mask:0xf bank_mask:0xf bound_ctrl:1
	s_nop 1
	v_add_f32_dpp v12, v12, v12 row_half_mirror row_mask:0xf bank_mask:0xf bound_ctrl:1
	s_nop 1
	v_add_f32_dpp v12, v12, v12 row_mirror row_mask:0xf bank_mask:0xf bound_ctrl:1
	v_mov_b32_e32 v18, v12
	s_nop 1
	v_permlane16_swap_b32_e32 v12, v18
	v_add_f32_e32 v12, v12, v18
	v_mov_b32_e32 v18, v12
	s_nop 1
	v_permlane32_swap_b32_e32 v12, v18
	v_pk_add_f32 v[12:13], v[12:13], v[18:19]
	s_nop 0
	v_pk_fma_f32 v[12:13], v[12:13], s[2:3], v[14:15] op_sel_hi:[1,0,0]
	s_nop 0
	v_mul_f32_e32 v14, 0x4b800000, v13
	v_cmp_gt_f32_e64 s[40:41], s37, v13
	v_cmp_gt_f32_e32 vcc, s37, v12
	s_nop 0
	v_cndmask_b32_e64 v13, v13, v14, s[40:41]
	v_rsq_f32_e32 v13, v13
	s_nop 0
	v_mul_f32_e32 v14, 0x45800000, v13
	v_cndmask_b32_e64 v13, v13, v14, s[40:41]
	v_mul_f32_e32 v14, v22, v13
	v_mul_f32_e32 v14, v9, v14
	v_bfe_u32 v15, v14, 16, 1
	v_mul_f32_e32 v13, v23, v13
	v_add3_u32 v14, v14, v15, s86
	v_mul_f32_e32 v13, v10, v13
	global_store_short_d16_hi v[16:17], v14, off offset:3584
	v_bfe_u32 v14, v13, 16, 1
	v_add3_u32 v13, v13, v14, s86
	global_store_short_d16_hi v[16:17], v13, off offset:3712
	v_mul_f32_e32 v13, 0x4b800000, v12
	v_cndmask_b32_e32 v12, v12, v13, vcc
	v_rsq_f32_e32 v12, v12
	s_nop 0
	v_mul_f32_e32 v13, 0x45800000, v12
	v_cndmask_b32_e32 v14, v12, v13, vcc
	v_mul_f32_e32 v12, v24, v14
	v_mul_f32_e32 v12, v9, v12
	v_bfe_u32 v13, v12, 16, 1
	v_mul_f32_e32 v11, v11, v14
	v_add3_u32 v15, v12, v13, s86
	v_lshl_add_u64 v[12:13], s[12:13], 0, v[0:1]
	v_mul_f32_e32 v11, v10, v11
	s_add_u32 s12, s12, s18
	v_add_co_u32_e32 v12, vcc, s1, v12
	v_bfe_u32 v14, v11, 16, 1
	s_addc_u32 s13, s13, s19
	v_addc_co_u32_e32 v13, vcc, 0, v13, vcc
	v_add3_u32 v11, v11, v14, s86
	s_cmpk_gt_i32 s14, 0x20ff
	global_store_short_d16_hi v[12:13], v15, off offset:3072
	global_store_short_d16_hi v[12:13], v11, off offset:3200
	s_cbranch_scc0 .LBB0_592
